# attention selected+window branches: PV MFMA operands swapped so each lane owns a q row; per-lane deferred rescale; epilogue packs bf16 and stores 16 B per lane instead of 64 2-byte stores
# baseline (speedup 1.0000x reference)
; __device__ __forceinline__ unsigned f2bf(float f) { unsigned u = __builtin_bit_cast(unsigned, f); return (u + 0x7fffu + ((u >> 16) & 1u)) >> 16; }
; __device__ __forceinline__ int crow(int r, int hi) { return (r & 3) + 8 * (r >> 2) + 4 * hi; }
; template <int MODE> ...
;     ...
;     asm volatile("s_waitcnt lgkmcnt(0)" ::: "memory");
;     if (hi == 0) wsl[32 + l32] = l_reg > 0.f ? 1.f / l_reg : 0.f;
;     asm volatile("s_waitcnt lgkmcnt(0)" ::: "memory");
; #pragma unroll
;     for (int r = 0; r < 16; ++r) { const int q = crow(r, hi); const float rli = wsl[32 + q]; bf16* op = Obase + (size_t)(8 * wave + (q >> 2)) * 2048 + (q & 3) * 128 + l32;
; #pragma unroll
;         for (int d0 = 0; d0 < 4; ++d0) op[d0 * 32] = (bf16)f2bf(o[d0][r] * rli); }
.LBB0_790:
	s_waitcnt lgkmcnt(0)
	s_add_u32 s0, s90, 0x4000000
	s_addc_u32 s1, s91, 0
	s_mov_b32 s2, 0x07060302
	v_lshrrev_b32_e32 v101, 2, v1
	v_lshl_or_b32 v101, s6, 3, v101
	v_lshlrev_b32_e32 v101, 12, v101
	v_and_b32_e32 v68, 3, v1
	v_lshl_or_b32 v101, v68, 8, v101
	v_lshl_or_b32 v101, v120, 4, v101
	v_mul_f32_e32 v92, v4, v2
	v_mul_f32_e32 v93, v5, v2
	v_mul_f32_e32 v94, v6, v2
	v_mul_f32_e32 v95, v7, v2
	v_bfe_u32 v96, v92, 16, 1
	v_bfe_u32 v97, v93, 16, 1
	v_bfe_u32 v98, v94, 16, 1
	v_bfe_u32 v99, v95, 16, 1
	v_add3_u32 v92, v92, v96, s72
	v_add3_u32 v93, v93, v97, s72
	v_add3_u32 v94, v94, v98, s72
	v_add3_u32 v95, v95, v99, s72
	v_perm_b32 v84, v93, v92, s2
	v_perm_b32 v85, v95, v94, s2
	v_mul_f32_e32 v92, v8, v2
	v_mul_f32_e32 v93, v9, v2
	v_mul_f32_e32 v94, v10, v2
	v_mul_f32_e32 v95, v11, v2
	v_bfe_u32 v96, v92, 16, 1
	v_bfe_u32 v97, v93, 16, 1
	v_bfe_u32 v98, v94, 16, 1
	v_bfe_u32 v99, v95, 16, 1
	v_add3_u32 v92, v92, v96, s72
	v_add3_u32 v93, v93, v97, s72
	v_add3_u32 v94, v94, v98, s72
	v_add3_u32 v95, v95, v99, s72
	v_perm_b32 v86, v93, v92, s2
	v_perm_b32 v87, v95, v94, s2
	v_mul_f32_e32 v92, v12, v2
	v_mul_f32_e32 v93, v13, v2
	v_mul_f32_e32 v94, v14, v2
	v_mul_f32_e32 v95, v15, v2
	v_bfe_u32 v96, v92, 16, 1
	v_bfe_u32 v97, v93, 16, 1
	v_bfe_u32 v98, v94, 16, 1
	v_bfe_u32 v99, v95, 16, 1
	v_add3_u32 v92, v92, v96, s72
	v_add3_u32 v93, v93, v97, s72
	v_add3_u32 v94, v94, v98, s72
	v_add3_u32 v95, v95, v99, s72
	v_perm_b32 v88, v93, v92, s2
	v_perm_b32 v89, v95, v94, s2
	v_mul_f32_e32 v92, v16, v2
	v_mul_f32_e32 v93, v17, v2
	v_mul_f32_e32 v94, v18, v2
	v_mul_f32_e32 v95, v19, v2
	v_bfe_u32 v96, v92, 16, 1
	v_bfe_u32 v97, v93, 16, 1
	v_bfe_u32 v98, v94, 16, 1
	v_bfe_u32 v99, v95, 16, 1
	v_add3_u32 v92, v92, v96, s72
	v_add3_u32 v93, v93, v97, s72
	v_add3_u32 v94, v94, v98, s72
	v_add3_u32 v95, v95, v99, s72
	v_perm_b32 v90, v93, v92, s2
	v_perm_b32 v91, v95, v94, s2
	s_nop 1
	v_permlane32_swap_b32_e32 v84, v86
	v_permlane32_swap_b32_e32 v85, v87
	v_permlane32_swap_b32_e32 v88, v90
	v_permlane32_swap_b32_e32 v89, v91
	global_store_dwordx4 v101, v[84:87], s[0:1] offset:0
	global_store_dwordx4 v101, v[88:91], s[0:1] offset:32
	s_nop 1
	v_mul_f32_e32 v92, v20, v2
	v_mul_f32_e32 v93, v21, v2
	v_mul_f32_e32 v94, v22, v2
	v_mul_f32_e32 v95, v23, v2
	v_bfe_u32 v96, v92, 16, 1
	v_bfe_u32 v97, v93, 16, 1
	v_bfe_u32 v98, v94, 16, 1
	v_bfe_u32 v99, v95, 16, 1
	v_add3_u32 v92, v92, v96, s72
	v_add3_u32 v93, v93, v97, s72
	v_add3_u32 v94, v94, v98, s72
	v_add3_u32 v95, v95, v99, s72
	v_perm_b32 v84, v93, v92, s2
	v_perm_b32 v85, v95, v94, s2
	v_mul_f32_e32 v92, v24, v2
	v_mul_f32_e32 v93, v25, v2
	v_mul_f32_e32 v94, v26, v2
	v_mul_f32_e32 v95, v27, v2
	v_bfe_u32 v96, v92, 16, 1
	v_bfe_u32 v97, v93, 16, 1
	v_bfe_u32 v98, v94, 16, 1
	v_bfe_u32 v99, v95, 16, 1
	v_add3_u32 v92, v92, v96, s72
	v_add3_u32 v93, v93, v97, s72
	v_add3_u32 v94, v94, v98, s72
	v_add3_u32 v95, v95, v99, s72
	v_perm_b32 v86, v93, v92, s2
	v_perm_b32 v87, v95, v94, s2
	v_mul_f32_e32 v92, v28, v2
	v_mul_f32_e32 v93, v29, v2
	v_mul_f32_e32 v94, v30, v2
	v_mul_f32_e32 v95, v31, v2
	v_bfe_u32 v96, v92, 16, 1
	v_bfe_u32 v97, v93, 16, 1
	v_bfe_u32 v98, v94, 16, 1
	v_bfe_u32 v99, v95, 16, 1
	v_add3_u32 v92, v92, v96, s72
	v_add3_u32 v93, v93, v97, s72
	v_add3_u32 v94, v94, v98, s72
	v_add3_u32 v95, v95, v99, s72
	v_perm_b32 v88, v93, v92, s2
	v_perm_b32 v89, v95, v94, s2
	v_mul_f32_e32 v92, v32, v2
	v_mul_f32_e32 v93, v33, v2
	v_mul_f32_e32 v94, v34, v2
	v_mul_f32_e32 v95, v35, v2
	v_bfe_u32 v96, v92, 16, 1
	v_bfe_u32 v97, v93, 16, 1
	v_bfe_u32 v98, v94, 16, 1
	v_bfe_u32 v99, v95, 16, 1
	v_add3_u32 v92, v92, v96, s72
	v_add3_u32 v93, v93, v97, s72
	v_add3_u32 v94, v94, v98, s72
	v_add3_u32 v95, v95, v99, s72
	v_perm_b32 v90, v93, v92, s2
	v_perm_b32 v91, v95, v94, s2
	s_nop 1
	v_permlane32_swap_b32_e32 v84, v86
	v_permlane32_swap_b32_e32 v85, v87
	v_permlane32_swap_b32_e32 v88, v90
	v_permlane32_swap_b32_e32 v89, v91
; __device__ __forceinline__ unsigned f2bf(float f) { unsigned u = __builtin_bit_cast(unsigned, f); return (u + 0x7fffu + ((u >> 16) & 1u)) >> 16; }
; __device__ __forceinline__ int crow(int r, int hi) { return (r & 3) + 8 * (r >> 2) + 4 * hi; }
; template <int MODE> ...
;     ...
;     for (int r = 0; r < 16; ++r) { const int q = crow(r, hi); const float rli = wsl[32 + q]; bf16* op = Obase + (size_t)(8 * wave + (q >> 2)) * 2048 + (q & 3) * 128 + l32;
; #pragma unroll
;         for (int d0 = 0; d0 < 4; ++d0) op[d0 * 32] = (bf16)f2bf(o[d0][r] * rli); }
; __global__ void __launch_bounds__(NWAVES * 64, 2) hybrid_fwd(Args args) {
;     ...
;             for (int u = F.vcu; u < 256; u += F.G) { const int g = u & 3, tbp = u >> 2;
; #pragma unroll 1
;                 for (int uu = 0; uu < 2; ++uu) attn_unit(F.lds + RING_OFF, g, uu ? tbp : 127 - tbp, PROJ, KC, VC, AO, tid); }
	global_store_dwordx4 v101, v[84:87], s[0:1] offset:64
	global_store_dwordx4 v101, v[88:91], s[0:1] offset:96
	s_nop 1
	v_mul_f32_e32 v92, v36, v2
	v_mul_f32_e32 v93, v37, v2
	v_mul_f32_e32 v94, v38, v2
	v_mul_f32_e32 v95, v39, v2
	v_bfe_u32 v96, v92, 16, 1
	v_bfe_u32 v97, v93, 16, 1
	v_bfe_u32 v98, v94, 16, 1
	v_bfe_u32 v99, v95, 16, 1
	v_add3_u32 v92, v92, v96, s72
	v_add3_u32 v93, v93, v97, s72
	v_add3_u32 v94, v94, v98, s72
	v_add3_u32 v95, v95, v99, s72
	v_perm_b32 v84, v93, v92, s2
	v_perm_b32 v85, v95, v94, s2
	v_mul_f32_e32 v92, v40, v2
	v_mul_f32_e32 v93, v41, v2
	v_mul_f32_e32 v94, v42, v2
	v_mul_f32_e32 v95, v43, v2
	v_bfe_u32 v96, v92, 16, 1
	v_bfe_u32 v97, v93, 16, 1
	v_bfe_u32 v98, v94, 16, 1
	v_bfe_u32 v99, v95, 16, 1
	v_add3_u32 v92, v92, v96, s72
	v_add3_u32 v93, v93, v97, s72
	v_add3_u32 v94, v94, v98, s72
	v_add3_u32 v95, v95, v99, s72
	v_perm_b32 v86, v93, v92, s2
	v_perm_b32 v87, v95, v94, s2
	v_mul_f32_e32 v92, v44, v2
	v_mul_f32_e32 v93, v45, v2
	v_mul_f32_e32 v94, v46, v2
	v_mul_f32_e32 v95, v47, v2
	v_bfe_u32 v96, v92, 16, 1
	v_bfe_u32 v97, v93, 16, 1
	v_bfe_u32 v98, v94, 16, 1
	v_bfe_u32 v99, v95, 16, 1
	v_add3_u32 v92, v92, v96, s72
	v_add3_u32 v93, v93, v97, s72
	v_add3_u32 v94, v94, v98, s72
	v_add3_u32 v95, v95, v99, s72
	v_perm_b32 v88, v93, v92, s2
	v_perm_b32 v89, v95, v94, s2
	v_mul_f32_e32 v92, v48, v2
	v_mul_f32_e32 v93, v49, v2
	v_mul_f32_e32 v94, v50, v2
	v_mul_f32_e32 v95, v51, v2
	v_bfe_u32 v96, v92, 16, 1
	v_bfe_u32 v97, v93, 16, 1
	v_bfe_u32 v98, v94, 16, 1
	v_bfe_u32 v99, v95, 16, 1
	v_add3_u32 v92, v92, v96, s72
	v_add3_u32 v93, v93, v97, s72
	v_add3_u32 v94, v94, v98, s72
	v_add3_u32 v95, v95, v99, s72
	v_perm_b32 v90, v93, v92, s2
	v_perm_b32 v91, v95, v94, s2
	s_nop 1
	v_permlane32_swap_b32_e32 v84, v86
	v_permlane32_swap_b32_e32 v85, v87
	v_permlane32_swap_b32_e32 v88, v90
	v_permlane32_swap_b32_e32 v89, v91
	global_store_dwordx4 v101, v[84:87], s[0:1] offset:128
	global_store_dwordx4 v101, v[88:91], s[0:1] offset:160
	s_nop 1
	v_mul_f32_e32 v92, v52, v2
	v_mul_f32_e32 v93, v53, v2
	v_mul_f32_e32 v94, v54, v2
	v_mul_f32_e32 v95, v55, v2
	v_bfe_u32 v96, v92, 16, 1
	v_bfe_u32 v97, v93, 16, 1
	v_bfe_u32 v98, v94, 16, 1
	v_bfe_u32 v99, v95, 16, 1
	v_add3_u32 v92, v92, v96, s72
	v_add3_u32 v93, v93, v97, s72
	v_add3_u32 v94, v94, v98, s72
	v_add3_u32 v95, v95, v99, s72
	v_perm_b32 v84, v93, v92, s2
	v_perm_b32 v85, v95, v94, s2
	v_mul_f32_e32 v92, v56, v2
	v_mul_f32_e32 v93, v57, v2
	v_mul_f32_e32 v94, v58, v2
	v_mul_f32_e32 v95, v59, v2
	v_bfe_u32 v96, v92, 16, 1
	v_bfe_u32 v97, v93, 16, 1
	v_bfe_u32 v98, v94, 16, 1
	v_bfe_u32 v99, v95, 16, 1
	v_add3_u32 v92, v92, v96, s72
	v_add3_u32 v93, v93, v97, s72
	v_add3_u32 v94, v94, v98, s72
	v_add3_u32 v95, v95, v99, s72
	v_perm_b32 v86, v93, v92, s2
	v_perm_b32 v87, v95, v94, s2
	v_mul_f32_e32 v92, v60, v2
	v_mul_f32_e32 v93, v61, v2
	v_mul_f32_e32 v94, v62, v2
	v_mul_f32_e32 v95, v63, v2
	v_bfe_u32 v96, v92, 16, 1
	v_bfe_u32 v97, v93, 16, 1
	v_bfe_u32 v98, v94, 16, 1
	v_bfe_u32 v99, v95, 16, 1
	v_add3_u32 v92, v92, v96, s72
	v_add3_u32 v93, v93, v97, s72
	v_add3_u32 v94, v94, v98, s72
	v_add3_u32 v95, v95, v99, s72
	v_perm_b32 v88, v93, v92, s2
	v_perm_b32 v89, v95, v94, s2
	v_mul_f32_e32 v92, v64, v2
	v_mul_f32_e32 v93, v65, v2
	v_mul_f32_e32 v94, v66, v2
	v_mul_f32_e32 v95, v67, v2
	v_bfe_u32 v96, v92, 16, 1
	v_bfe_u32 v97, v93, 16, 1
	v_bfe_u32 v98, v94, 16, 1
	v_bfe_u32 v99, v95, 16, 1
	v_add3_u32 v92, v92, v96, s72
	v_add3_u32 v93, v93, v97, s72
	v_add3_u32 v94, v94, v98, s72
	v_add3_u32 v95, v95, v99, s72
	v_perm_b32 v90, v93, v92, s2
	v_perm_b32 v91, v95, v94, s2
	s_nop 1
	v_permlane32_swap_b32_e32 v84, v86
	v_permlane32_swap_b32_e32 v85, v87
	v_permlane32_swap_b32_e32 v88, v90
	v_permlane32_swap_b32_e32 v89, v91
	global_store_dwordx4 v101, v[84:87], s[0:1] offset:192
	global_store_dwordx4 v101, v[88:91], s[0:1] offset:224
	s_nop 1
	s_mov_b64 s[6:7], 0
	s_and_b64 vcc, exec, s[96:97]
	s_waitcnt vmcnt(0)
	s_barrier
	s_cbranch_vccnz .LBB0_788

; __device__ __forceinline__ int crow(int r, int hi) { return (r & 3) + 8 * (r >> 2) + 4 * hi; }
; __device__ __forceinline__ float at_softmax(f32x16& p0, f32x16& p1, float& m_reg, f32x16& negm, float& l_reg, bf16x8& pa0, bf16x8& pa1, bf16x8& pa2, bf16x8& pa3, bool rowsel, bool use_rowsel) {
;     ...
;     float s0 = 0.f, s1 = 0.f, s2 = 0.f, s3 = 0.f;
; #pragma unroll
;     for (int r = 0; r < 16; r += 4) { p0[r] = __builtin_amdgcn_exp2f(p0[r]); p0[r + 1] = __builtin_amdgcn_exp2f(p0[r + 1]); p0[r + 2] = __builtin_amdgcn_exp2f(p0[r + 2]); p0[r + 3] = __builtin_amdgcn_exp2f(p0[r + 3]);
;         s0 += p0[r]; s1 += p0[r + 1]; s2 += p0[r + 2]; s3 += p0[r + 3]; }
; #pragma unroll
;     for (int r = 0; r < 16; r += 4) { p1[r] = __builtin_amdgcn_exp2f(p1[r]); p1[r + 1] = __builtin_amdgcn_exp2f(p1[r + 1]); p1[r + 2] = __builtin_amdgcn_exp2f(p1[r + 2]); p1[r + 3] = __builtin_amdgcn_exp2f(p1[r + 3]);
;         s0 += p1[r]; s1 += p1[r + 1]; s2 += p1[r + 2]; s3 += p1[r + 3]; }
;     float ps = (s0 + s1) + (s2 + s3);
;     if (use_rowsel && !rowsel) ps = 0.f;
;     { auto rr = __builtin_amdgcn_permlane32_swap(__float_as_uint(ps), __float_as_uint(ps), false, false); ps = __uint_as_float(rr[0]) + __uint_as_float(rr[1]); }
;     l_reg = l_reg * alpha + ps;
;     const unsigned keep = (use_rowsel && !rowsel) ? 0u : 0xffffffffu;
;     ...
;     PK4(p0, 0, pa0); PK4(p0, 8, pa1); PK4(p1, 0, pa2); PK4(p1, 8, pa3);
; template <int MODE> ...
;     ...
;         if (__any(alpha < 1.f)) { if (hi == 0) wsl[l32] = alpha; asm volatile("s_waitcnt lgkmcnt(0)" ::: "memory");
; #pragma unroll
;             for (int d = 0; d < 4; ++d)
; #pragma unroll
;                 for (int r = 0; r < 16; ++r) o[d][r] *= wsl[crow(r, hi)]; }
.LBB0_854:
	v_exp_f32_e32 v4, v114
	v_exp_f32_e32 v5, v115
	v_exp_f32_e32 v6, v116
	v_exp_f32_e32 v7, v117
	v_exp_f32_e32 v12, v118
	v_exp_f32_e32 v13, v119
	v_exp_f32_e32 v14, v120
	v_exp_f32_e32 v15, v121
	v_exp_f32_e32 v114, v122
	v_exp_f32_e32 v115, v123
	v_exp_f32_e32 v116, v124
	v_exp_f32_e32 v117, v125
	v_exp_f32_e32 v118, v126
	v_exp_f32_e32 v119, v127
	v_exp_f32_e32 v120, v128
	v_exp_f32_e32 v121, v129
	v_add_f32_e32 v8, 0, v4
	v_add_f32_e32 v9, 0, v5
	v_add_f32_e32 v10, 0, v6
	v_add_f32_e32 v11, 0, v7
	v_exp_f32_e32 v98, v98
	v_exp_f32_e32 v99, v99
	v_exp_f32_e32 v100, v100
	v_exp_f32_e32 v101, v101
	v_add_f32_e32 v8, v12, v8
	v_add_f32_e32 v9, v13, v9
	v_add_f32_e32 v10, v14, v10
	v_add_f32_e32 v11, v15, v11
	v_exp_f32_e32 v102, v102
	v_exp_f32_e32 v103, v103
	v_exp_f32_e32 v104, v104
	v_exp_f32_e32 v105, v105
	v_add_f32_e32 v8, v114, v8
	v_add_f32_e32 v9, v115, v9
	v_add_f32_e32 v10, v116, v10
	v_add_f32_e32 v11, v117, v11
	v_exp_f32_e32 v106, v106
	v_exp_f32_e32 v107, v107
	v_exp_f32_e32 v108, v108
	v_exp_f32_e32 v109, v109
	v_add_f32_e32 v8, v118, v8
	v_add_f32_e32 v9, v119, v9
	v_add_f32_e32 v10, v120, v10
	v_add_f32_e32 v11, v121, v11
	v_exp_f32_e32 v110, v110
	v_exp_f32_e32 v111, v111
	v_exp_f32_e32 v112, v112
	v_exp_f32_e32 v113, v113
	v_add_f32_e32 v8, v98, v8
	v_add_f32_e32 v9, v99, v9
	v_add_f32_e32 v10, v100, v10
	v_add_f32_e32 v11, v101, v11
	v_add_f32_e32 v8, v102, v8
	v_add_f32_e32 v9, v103, v9
	v_add_f32_e32 v10, v104, v10
	v_add_f32_e32 v11, v105, v11
	v_add_f32_e32 v8, v106, v8
	v_add_f32_e32 v9, v107, v9
	v_add_f32_e32 v10, v108, v10
	v_add_f32_e32 v11, v109, v11
	v_add_f32_e32 v8, v110, v8
	v_add_f32_e32 v9, v111, v9
	v_add_f32_e32 v10, v112, v10
	v_add_f32_e32 v11, v113, v11
	v_add_f32_e32 v8, v9, v8
	v_add_f32_e32 v9, v11, v10
	v_add_f32_e32 v8, v9, v8
	v_cndmask_b32_e64 v16, 0, v8, s[6:7]
	v_cvt_pk_bf16_f32 v4, v4, v5
	v_cvt_pk_bf16_f32 v5, v6, v7
	v_cvt_pk_bf16_f32 v6, v12, v13
	v_cvt_pk_bf16_f32 v7, v14, v15
	v_cvt_pk_bf16_f32 v8, v114, v115
	v_cvt_pk_bf16_f32 v9, v116, v117
	v_cvt_pk_bf16_f32 v10, v118, v119
	v_cvt_pk_bf16_f32 v11, v120, v121
	v_mov_b32_e32 v17, v16
	v_cndmask_b32_e64 v15, 0, v11, s[6:7]
	v_cndmask_b32_e64 v14, 0, v10, s[6:7]
	v_cndmask_b32_e64 v13, 0, v9, s[6:7]
	v_cndmask_b32_e64 v12, 0, v8, s[6:7]
	v_cvt_pk_bf16_f32 v8, v98, v99
	v_cvt_pk_bf16_f32 v9, v100, v101
	v_cvt_pk_bf16_f32 v10, v102, v103
	v_cvt_pk_bf16_f32 v11, v104, v105
	v_cndmask_b32_e64 v7, 0, v7, s[6:7]
	v_cndmask_b32_e64 v101, 0, v11, s[6:7]
	v_cndmask_b32_e64 v100, 0, v10, s[6:7]
	v_cndmask_b32_e64 v99, 0, v9, s[6:7]
	v_cndmask_b32_e64 v98, 0, v8, s[6:7]
	v_cvt_pk_bf16_f32 v8, v106, v107
	v_cvt_pk_bf16_f32 v9, v108, v109
	v_cvt_pk_bf16_f32 v10, v110, v111
	v_cvt_pk_bf16_f32 v11, v112, v113
	v_cndmask_b32_e64 v6, 0, v6, s[6:7]
	v_cndmask_b32_e64 v5, 0, v5, s[6:7]
	v_cndmask_b32_e64 v4, 0, v4, s[6:7]
	v_cndmask_b32_e64 v11, 0, v11, s[6:7]
	v_cndmask_b32_e64 v10, 0, v10, s[6:7]
	v_cndmask_b32_e64 v9, 0, v9, s[6:7]
	v_cndmask_b32_e64 v8, 0, v8, s[6:7]
	v_permlane32_swap_b32_e32 v16, v17
	v_permlane32_swap_b32_e32 v4, v6
	v_permlane32_swap_b32_e32 v5, v7
	v_permlane32_swap_b32_e32 v12, v14
	v_permlane32_swap_b32_e32 v13, v15
	v_permlane32_swap_b32_e32 v98, v100
	v_permlane32_swap_b32_e32 v99, v101
	v_permlane32_swap_b32_e32 v8, v10
	v_permlane32_swap_b32_e32 v9, v11
	v_cmp_gt_f32_e32 vcc, 1.0, v2
	s_cbranch_vccz .LBB0_858
	v_pk_mul_f32 v[66:67], v[66:67], v[2:3] op_sel_hi:[1,0]
	v_pk_mul_f32 v[68:69], v[68:69], v[2:3] op_sel_hi:[1,0]
	v_pk_mul_f32 v[70:71], v[70:71], v[2:3] op_sel_hi:[1,0]
	v_pk_mul_f32 v[72:73], v[72:73], v[2:3] op_sel_hi:[1,0]
	v_pk_mul_f32 v[74:75], v[74:75], v[2:3] op_sel_hi:[1,0]
	v_pk_mul_f32 v[76:77], v[76:77], v[2:3] op_sel_hi:[1,0]
	v_pk_mul_f32 v[78:79], v[78:79], v[2:3] op_sel_hi:[1,0]
	v_pk_mul_f32 v[80:81], v[80:81], v[2:3] op_sel_hi:[1,0]
	v_pk_mul_f32 v[50:51], v[50:51], v[2:3] op_sel_hi:[1,0]
	v_pk_mul_f32 v[52:53], v[52:53], v[2:3] op_sel_hi:[1,0]
	v_pk_mul_f32 v[54:55], v[54:55], v[2:3] op_sel_hi:[1,0]
	v_pk_mul_f32 v[56:57], v[56:57], v[2:3] op_sel_hi:[1,0]
	v_pk_mul_f32 v[58:59], v[58:59], v[2:3] op_sel_hi:[1,0]
	v_pk_mul_f32 v[60:61], v[60:61], v[2:3] op_sel_hi:[1,0]
	v_pk_mul_f32 v[62:63], v[62:63], v[2:3] op_sel_hi:[1,0]
	v_pk_mul_f32 v[64:65], v[64:65], v[2:3] op_sel_hi:[1,0]
	v_pk_mul_f32 v[34:35], v[34:35], v[2:3] op_sel_hi:[1,0]
	v_pk_mul_f32 v[36:37], v[36:37], v[2:3] op_sel_hi:[1,0]
	v_pk_mul_f32 v[38:39], v[38:39], v[2:3] op_sel_hi:[1,0]
	v_pk_mul_f32 v[40:41], v[40:41], v[2:3] op_sel_hi:[1,0]
	v_pk_mul_f32 v[42:43], v[42:43], v[2:3] op_sel_hi:[1,0]
	v_pk_mul_f32 v[44:45], v[44:45], v[2:3] op_sel_hi:[1,0]
	v_pk_mul_f32 v[46:47], v[46:47], v[2:3] op_sel_hi:[1,0]
	v_pk_mul_f32 v[48:49], v[48:49], v[2:3] op_sel_hi:[1,0]
	v_pk_mul_f32 v[18:19], v[18:19], v[2:3] op_sel_hi:[1,0]
	v_pk_mul_f32 v[20:21], v[20:21], v[2:3] op_sel_hi:[1,0]
	v_pk_mul_f32 v[22:23], v[22:23], v[2:3] op_sel_hi:[1,0]
	v_pk_mul_f32 v[24:25], v[24:25], v[2:3] op_sel_hi:[1,0]
	v_pk_mul_f32 v[26:27], v[26:27], v[2:3] op_sel_hi:[1,0]
	v_pk_mul_f32 v[28:29], v[28:29], v[2:3] op_sel_hi:[1,0]
	v_pk_mul_f32 v[30:31], v[30:31], v[2:3] op_sel_hi:[1,0]
	v_pk_mul_f32 v[32:33], v[32:33], v[2:3] op_sel_hi:[1,0]
; __device__ __forceinline__ void at_pv(f32x16 (&o)[4], int vb, bf16x8 pa0, bf16x8 pa1, bf16x8 pa2, bf16x8 pa3) {
;     ...
;     PV_D0(0); PV_D0(1); PV_D0(2); PV_D0(3);
;     ...
; }
; __device__ __forceinline__ float at_softmax(f32x16& p0, f32x16& p1, float& m_reg, f32x16& negm, float& l_reg, bf16x8& pa0, bf16x8& pa1, bf16x8& pa2, bf16x8& pa3, bool rowsel, bool use_rowsel) {
;     ...
;     l_reg = l_reg * alpha + ps;
.LBB0_858:
	v_add_f32_e32 v16, v16, v17
	v_fmac_f32_e32 v16, v201, v2
	v_add_u32_e32 v2, s17, v199
	ds_read_b64_tr_b16 v[102:103], v2 offset:0
	ds_read_b64_tr_b16 v[104:105], v2 offset:0x800
	ds_read_b64_tr_b16 v[106:107], v2 offset:0x1000
	ds_read_b64_tr_b16 v[108:109], v2 offset:0x1800
	ds_read_b64_tr_b16 v[110:111], v2 offset:0x2000
	ds_read_b64_tr_b16 v[112:113], v2 offset:0x2800
	ds_read_b64_tr_b16 v[114:115], v2 offset:0x3000
	ds_read_b64_tr_b16 v[116:117], v2 offset:0x3800
	s_waitcnt lgkmcnt(0)
	s_nop 0
	v_mfma_f32_32x32x16_bf16 v[66:81], v[102:105], v[4:7], v[66:81]
	ds_read_b64_tr_b16 v[102:103], v2 offset:0x200
	ds_read_b64_tr_b16 v[104:105], v2 offset:0xa00
	v_mfma_f32_32x32x16_bf16 v[66:81], v[106:109], v[12:15], v[66:81]
	ds_read_b64_tr_b16 v[106:107], v2 offset:0x1200
	ds_read_b64_tr_b16 v[108:109], v2 offset:0x1a00
	v_mfma_f32_32x32x16_bf16 v[66:81], v[110:113], v[98:101], v[66:81]
	ds_read_b64_tr_b16 v[110:111], v2 offset:0x2200
	ds_read_b64_tr_b16 v[112:113], v2 offset:0x2a00
	v_mfma_f32_32x32x16_bf16 v[66:81], v[114:117], v[8:11], v[66:81]
	ds_read_b64_tr_b16 v[114:115], v2 offset:0x3200
	ds_read_b64_tr_b16 v[116:117], v2 offset:0x3a00
	s_waitcnt lgkmcnt(0)
	v_mfma_f32_32x32x16_bf16 v[50:65], v[102:105], v[4:7], v[50:65]
	ds_read_b64_tr_b16 v[102:103], v2 offset:0x400
	ds_read_b64_tr_b16 v[104:105], v2 offset:0xc00
	v_mfma_f32_32x32x16_bf16 v[50:65], v[106:109], v[12:15], v[50:65]
	ds_read_b64_tr_b16 v[106:107], v2 offset:0x1400
	ds_read_b64_tr_b16 v[108:109], v2 offset:0x1c00
	v_mfma_f32_32x32x16_bf16 v[50:65], v[110:113], v[98:101], v[50:65]
	ds_read_b64_tr_b16 v[110:111], v2 offset:0x2400
	ds_read_b64_tr_b16 v[112:113], v2 offset:0x2c00
	v_mfma_f32_32x32x16_bf16 v[50:65], v[114:117], v[8:11], v[50:65]
	ds_read_b64_tr_b16 v[114:115], v2 offset:0x3400
	ds_read_b64_tr_b16 v[116:117], v2 offset:0x3c00
	s_waitcnt lgkmcnt(0)
	v_mfma_f32_32x32x16_bf16 v[34:49], v[102:105], v[4:7], v[34:49]
	ds_read_b64_tr_b16 v[102:103], v2 offset:0x600
	ds_read_b64_tr_b16 v[104:105], v2 offset:0xe00
	v_mfma_f32_32x32x16_bf16 v[34:49], v[106:109], v[12:15], v[34:49]
	ds_read_b64_tr_b16 v[106:107], v2 offset:0x1600
	ds_read_b64_tr_b16 v[108:109], v2 offset:0x1e00
	v_mfma_f32_32x32x16_bf16 v[34:49], v[110:113], v[98:101], v[34:49]
	ds_read_b64_tr_b16 v[110:111], v2 offset:0x2600
	ds_read_b64_tr_b16 v[112:113], v2 offset:0x2e00
	v_mfma_f32_32x32x16_bf16 v[34:49], v[114:117], v[8:11], v[34:49]
	ds_read_b64_tr_b16 v[114:115], v2 offset:0x3600
	ds_read_b64_tr_b16 v[116:117], v2 offset:0x3e00
	s_waitcnt lgkmcnt(0)
	v_mfma_f32_32x32x16_bf16 v[18:33], v[102:105], v[4:7], v[18:33]
	v_mov_b32_e32 v201, v16
	v_mfma_f32_32x32x16_bf16 v[18:33], v[106:109], v[12:15], v[18:33]
	v_mfma_f32_32x32x16_bf16 v[18:33], v[110:113], v[98:101], v[18:33]
	v_mfma_f32_32x32x16_bf16 v[18:33], v[114:117], v[8:11], v[18:33]

; __device__ __forceinline__ unsigned f2bf(float f) { unsigned u = __builtin_bit_cast(unsigned, f); return (u + 0x7fffu + ((u >> 16) & 1u)) >> 16; }
; __device__ __forceinline__ int crow(int r, int hi) { return (r & 3) + 8 * (r >> 2) + 4 * hi; }
; template <int MODE> ...
;     ...
;     asm volatile("s_waitcnt lgkmcnt(0)" ::: "memory");
;     if (hi == 0) wsl[32 + l32] = l_reg > 0.f ? 1.f / l_reg : 0.f;
;     asm volatile("s_waitcnt lgkmcnt(0)" ::: "memory");
; #pragma unroll
;     for (int r = 0; r < 16; ++r) { const int q = crow(r, hi); const float rli = wsl[32 + q]; bf16* op = Obase + (size_t)(8 * wave + (q >> 2)) * 2048 + (q & 3) * 128 + l32;
; #pragma unroll
;         for (int d0 = 0; d0 < 4; ++d0) op[d0 * 32] = (bf16)f2bf(o[d0][r] * rli); }
.LBB0_862:
	s_waitcnt lgkmcnt(0)
	v_div_scale_f32 v2, s[2:3], v201, v201, 1.0
	v_rcp_f32_e32 v4, v2
	v_div_scale_f32 v5, vcc, 1.0, v201, 1.0
	v_fma_f32 v6, -v2, v4, 1.0
	v_fmac_f32_e32 v4, v6, v4
	v_mul_f32_e32 v6, v5, v4
	v_fma_f32 v7, -v2, v6, v5
	v_fmac_f32_e32 v6, v7, v4
	v_fma_f32 v2, -v2, v6, v5
	v_div_fmas_f32 v2, v2, v4, v6
	v_div_fixup_f32 v2, v2, v201, 1.0
	v_cmp_lt_f32_e32 vcc, 0, v201
	s_nop 1
	v_cndmask_b32_e32 v2, 0, v2, vcc
	s_add_u32 s0, s90, 0x2000000
	s_addc_u32 s1, s91, 0
	s_mov_b32 s6, 0x07060302
	v_lshrrev_b32_e32 v100, 2, v1
	v_lshl_or_b32 v100, s8, 3, v100
	v_lshlrev_b32_e32 v100, 12, v100
	v_and_b32_e32 v4, 3, v1
	v_lshl_or_b32 v100, v4, 8, v100
	v_lshl_or_b32 v100, v188, 4, v100
	v_mul_f32_e32 v92, v66, v2
	v_mul_f32_e32 v93, v67, v2
	v_mul_f32_e32 v94, v68, v2
	v_mul_f32_e32 v95, v69, v2
	v_bfe_u32 v96, v92, 16, 1
	v_bfe_u32 v97, v93, 16, 1
	v_bfe_u32 v98, v94, 16, 1
	v_bfe_u32 v99, v95, 16, 1
	v_add3_u32 v92, v92, v96, s72
	v_add3_u32 v93, v93, v97, s72
	v_add3_u32 v94, v94, v98, s72
	v_add3_u32 v95, v95, v99, s72
	v_perm_b32 v84, v93, v92, s6
	v_perm_b32 v85, v95, v94, s6
	v_mul_f32_e32 v92, v70, v2
	v_mul_f32_e32 v93, v71, v2
	v_mul_f32_e32 v94, v72, v2
	v_mul_f32_e32 v95, v73, v2
	v_bfe_u32 v96, v92, 16, 1
	v_bfe_u32 v97, v93, 16, 1
	v_bfe_u32 v98, v94, 16, 1
	v_bfe_u32 v99, v95, 16, 1
	v_add3_u32 v92, v92, v96, s72
	v_add3_u32 v93, v93, v97, s72
	v_add3_u32 v94, v94, v98, s72
	v_add3_u32 v95, v95, v99, s72
	v_perm_b32 v86, v93, v92, s6
	v_perm_b32 v87, v95, v94, s6
	v_mul_f32_e32 v92, v74, v2
	v_mul_f32_e32 v93, v75, v2
	v_mul_f32_e32 v94, v76, v2
	v_mul_f32_e32 v95, v77, v2
	v_bfe_u32 v96, v92, 16, 1
	v_bfe_u32 v97, v93, 16, 1
	v_bfe_u32 v98, v94, 16, 1
	v_bfe_u32 v99, v95, 16, 1
	v_add3_u32 v92, v92, v96, s72
	v_add3_u32 v93, v93, v97, s72
	v_add3_u32 v94, v94, v98, s72
	v_add3_u32 v95, v95, v99, s72
	v_perm_b32 v88, v93, v92, s6
	v_perm_b32 v89, v95, v94, s6
	v_mul_f32_e32 v92, v78, v2
	v_mul_f32_e32 v93, v79, v2
	v_mul_f32_e32 v94, v80, v2
	v_mul_f32_e32 v95, v81, v2
	v_bfe_u32 v96, v92, 16, 1
	v_bfe_u32 v97, v93, 16, 1
	v_bfe_u32 v98, v94, 16, 1
	v_bfe_u32 v99, v95, 16, 1
	v_add3_u32 v92, v92, v96, s72
	v_add3_u32 v93, v93, v97, s72
	v_add3_u32 v94, v94, v98, s72
	v_add3_u32 v95, v95, v99, s72
	v_perm_b32 v90, v93, v92, s6
	v_perm_b32 v91, v95, v94, s6
	s_nop 1
	v_permlane32_swap_b32_e32 v84, v86
	v_permlane32_swap_b32_e32 v85, v87
	v_permlane32_swap_b32_e32 v88, v90
	v_permlane32_swap_b32_e32 v89, v91
	global_store_dwordx4 v100, v[84:87], s[0:1] offset:0
	global_store_dwordx4 v100, v[88:91], s[0:1] offset:32
	s_nop 1
	v_mul_f32_e32 v92, v50, v2
	v_mul_f32_e32 v93, v51, v2
	v_mul_f32_e32 v94, v52, v2
	v_mul_f32_e32 v95, v53, v2
	v_bfe_u32 v96, v92, 16, 1
	v_bfe_u32 v97, v93, 16, 1
	v_bfe_u32 v98, v94, 16, 1
	v_bfe_u32 v99, v95, 16, 1
	v_add3_u32 v92, v92, v96, s72
	v_add3_u32 v93, v93, v97, s72
	v_add3_u32 v94, v94, v98, s72
	v_add3_u32 v95, v95, v99, s72
	v_perm_b32 v84, v93, v92, s6
	v_perm_b32 v85, v95, v94, s6
	v_mul_f32_e32 v92, v54, v2
	v_mul_f32_e32 v93, v55, v2
	v_mul_f32_e32 v94, v56, v2
	v_mul_f32_e32 v95, v57, v2
	v_bfe_u32 v96, v92, 16, 1
	v_bfe_u32 v97, v93, 16, 1
	v_bfe_u32 v98, v94, 16, 1
	v_bfe_u32 v99, v95, 16, 1
	v_add3_u32 v92, v92, v96, s72
	v_add3_u32 v93, v93, v97, s72
	v_add3_u32 v94, v94, v98, s72
	v_add3_u32 v95, v95, v99, s72
	v_perm_b32 v86, v93, v92, s6
	v_perm_b32 v87, v95, v94, s6
	v_mul_f32_e32 v92, v58, v2
	v_mul_f32_e32 v93, v59, v2
	v_mul_f32_e32 v94, v60, v2
	v_mul_f32_e32 v95, v61, v2
	v_bfe_u32 v96, v92, 16, 1
	v_bfe_u32 v97, v93, 16, 1
	v_bfe_u32 v98, v94, 16, 1
	v_bfe_u32 v99, v95, 16, 1
	v_add3_u32 v92, v92, v96, s72
	v_add3_u32 v93, v93, v97, s72
	v_add3_u32 v94, v94, v98, s72
	v_add3_u32 v95, v95, v99, s72
	v_perm_b32 v88, v93, v92, s6
	v_perm_b32 v89, v95, v94, s6
	v_mul_f32_e32 v92, v62, v2
	v_mul_f32_e32 v93, v63, v2
	v_mul_f32_e32 v94, v64, v2
	v_mul_f32_e32 v95, v65, v2
	v_bfe_u32 v96, v92, 16, 1
	v_bfe_u32 v97, v93, 16, 1
	v_bfe_u32 v98, v94, 16, 1
	v_bfe_u32 v99, v95, 16, 1
	v_add3_u32 v92, v92, v96, s72
	v_add3_u32 v93, v93, v97, s72
	v_add3_u32 v94, v94, v98, s72
	v_add3_u32 v95, v95, v99, s72
	v_perm_b32 v90, v93, v92, s6
	v_perm_b32 v91, v95, v94, s6
	s_nop 1
	v_permlane32_swap_b32_e32 v84, v86
	v_permlane32_swap_b32_e32 v85, v87
	v_permlane32_swap_b32_e32 v88, v90
	v_permlane32_swap_b32_e32 v89, v91
	global_store_dwordx4 v100, v[84:87], s[0:1] offset:64
	global_store_dwordx4 v100, v[88:91], s[0:1] offset:96
	s_nop 1
	v_mul_f32_e32 v92, v34, v2
	v_mul_f32_e32 v93, v35, v2
	v_mul_f32_e32 v94, v36, v2
	v_mul_f32_e32 v95, v37, v2
	v_bfe_u32 v96, v92, 16, 1
	v_bfe_u32 v97, v93, 16, 1
	v_bfe_u32 v98, v94, 16, 1
	v_bfe_u32 v99, v95, 16, 1
	v_add3_u32 v92, v92, v96, s72
	v_add3_u32 v93, v93, v97, s72
	v_add3_u32 v94, v94, v98, s72
	v_add3_u32 v95, v95, v99, s72
	v_perm_b32 v84, v93, v92, s6
	v_perm_b32 v85, v95, v94, s6
	v_mul_f32_e32 v92, v38, v2
	v_mul_f32_e32 v93, v39, v2
	v_mul_f32_e32 v94, v40, v2
	v_mul_f32_e32 v95, v41, v2
	v_bfe_u32 v96, v92, 16, 1
	v_bfe_u32 v97, v93, 16, 1
	v_bfe_u32 v98, v94, 16, 1
	v_bfe_u32 v99, v95, 16, 1
; #define LAS __attribute__((address_space(3)))
; __device__ __forceinline__ unsigned f2bf(float f) { unsigned u = __builtin_bit_cast(unsigned, f); return (u + 0x7fffu + ((u >> 16) & 1u)) >> 16; }
; __device__ __forceinline__ int crow(int r, int hi) { return (r & 3) + 8 * (r >> 2) + 4 * hi; }
; __device__ __forceinline__ int v_rd_base(int lane) { return ((lane & 3) << 3) | (((lane >> 2) & 3) << 6) | (((lane >> 4) & 1) << 5) | (((lane >> 5) & 1) << 8); }
; template <int MODE> ...
;     int tid = tid_in; asm volatile("" : "+v"(tid));
;     const int lane = tid & 63, wave = __builtin_amdgcn_readfirstlane(tid >> 6), l32 = lane & 31, hi = lane >> 5;
;     LAS unsigned char* K_lds = lds + AT_K; LAS unsigned char* V_lds = lds + AT_V;
;     LAS float* wsl = (LAS float*)(lds + AT_WS) + wave * 64;
;     const int vb0 = (int)(unsigned)(size_t)V_lds + v_rd_base(lane);
;     const int ksr = tid >> 4, kslc = (tid & 15) ^ (ksr & 7);
;     const int vkk = (tid >> 7) * 8 + ((tid & 31) >> 2), vk = (vkk & ~0xC) | ((vkk & 4) << 1) | ((vkk & 8) >> 1), vc = ((tid >> 5) & 3) * 32 + (tid & 3) * 8;
;     const char* ksrc = (const char*)(Kb + (size_t)ksr * ld + 8 * kslc); const char* vsrc = (const char*)(Vb + (size_t)vk * ld + vc);
;     const size_t half_b = (size_t)32 * ld * 2, tile_b = (size_t)64 * ld * 2; const unsigned ldsw = (unsigned)wave * 1024u;
;     ...
;     float m_reg = -1e4f, l_reg = 0.f; f32x16 o[4] = {};
;     f32x16 negm;
; #pragma unroll
;     for (int r = 0; r < 16; ++r) negm[r] = 1e4f;
;     const int tq_min = __builtin_amdgcn_readfirstlane(tq), lim_min = (tq_min - 31) >> 4;
;     asm volatile("s_waitcnt vmcnt(0) lgkmcnt(0)" ::: "memory"); __builtin_amdgcn_s_barrier(); asm volatile("" ::: "memory");
;     AT_ISSUE(jlo, 0); if (NT > 1) AT_ISSUE(jlo + 1, 1);
;     ...
;     for (int r = 0; r < 16; ++r) { const int q = crow(r, hi); const float rli = wsl[32 + q]; bf16* op = Obase + (size_t)(8 * wave + (q >> 2)) * 2048 + (q & 3) * 128 + l32;
; #pragma unroll
;         for (int d0 = 0; d0 < 4; ++d0) op[d0 * 32] = (bf16)f2bf(o[d0][r] * rli); }
	v_add3_u32 v92, v92, v96, s72
	v_add3_u32 v93, v93, v97, s72
	v_add3_u32 v94, v94, v98, s72
	v_add3_u32 v95, v95, v99, s72
	v_perm_b32 v86, v93, v92, s6
	v_perm_b32 v87, v95, v94, s6
	v_mul_f32_e32 v92, v42, v2
	v_mul_f32_e32 v93, v43, v2
	v_mul_f32_e32 v94, v44, v2
	v_mul_f32_e32 v95, v45, v2
	v_bfe_u32 v96, v92, 16, 1
	v_bfe_u32 v97, v93, 16, 1
	v_bfe_u32 v98, v94, 16, 1
	v_bfe_u32 v99, v95, 16, 1
	v_add3_u32 v92, v92, v96, s72
	v_add3_u32 v93, v93, v97, s72
	v_add3_u32 v94, v94, v98, s72
	v_add3_u32 v95, v95, v99, s72
	v_perm_b32 v88, v93, v92, s6
	v_perm_b32 v89, v95, v94, s6
	v_mul_f32_e32 v92, v46, v2
	v_mul_f32_e32 v93, v47, v2
	v_mul_f32_e32 v94, v48, v2
	v_mul_f32_e32 v95, v49, v2
	v_bfe_u32 v96, v92, 16, 1
	v_bfe_u32 v97, v93, 16, 1
	v_bfe_u32 v98, v94, 16, 1
	v_bfe_u32 v99, v95, 16, 1
	v_add3_u32 v92, v92, v96, s72
	v_add3_u32 v93, v93, v97, s72
	v_add3_u32 v94, v94, v98, s72
	v_add3_u32 v95, v95, v99, s72
	v_perm_b32 v90, v93, v92, s6
	v_perm_b32 v91, v95, v94, s6
	s_nop 1
	v_permlane32_swap_b32_e32 v84, v86
	v_permlane32_swap_b32_e32 v85, v87
	v_permlane32_swap_b32_e32 v88, v90
	v_permlane32_swap_b32_e32 v89, v91
	global_store_dwordx4 v100, v[84:87], s[0:1] offset:128
	global_store_dwordx4 v100, v[88:91], s[0:1] offset:160
	s_nop 1
	v_mul_f32_e32 v92, v18, v2
	v_mul_f32_e32 v93, v19, v2
	v_mul_f32_e32 v94, v20, v2
	v_mul_f32_e32 v95, v21, v2
	v_bfe_u32 v96, v92, 16, 1
	v_bfe_u32 v97, v93, 16, 1
	v_bfe_u32 v98, v94, 16, 1
	v_bfe_u32 v99, v95, 16, 1
	v_add3_u32 v92, v92, v96, s72
	v_add3_u32 v93, v93, v97, s72
	v_add3_u32 v94, v94, v98, s72
	v_add3_u32 v95, v95, v99, s72
	v_perm_b32 v84, v93, v92, s6
	v_perm_b32 v85, v95, v94, s6
	v_mul_f32_e32 v92, v22, v2
	v_mul_f32_e32 v93, v23, v2
	v_mul_f32_e32 v94, v24, v2
	v_mul_f32_e32 v95, v25, v2
	v_bfe_u32 v96, v92, 16, 1
	v_bfe_u32 v97, v93, 16, 1
	v_bfe_u32 v98, v94, 16, 1
	v_bfe_u32 v99, v95, 16, 1
	v_add3_u32 v92, v92, v96, s72
	v_add3_u32 v93, v93, v97, s72
	v_add3_u32 v94, v94, v98, s72
	v_add3_u32 v95, v95, v99, s72
	v_perm_b32 v86, v93, v92, s6
	v_perm_b32 v87, v95, v94, s6
	v_mul_f32_e32 v92, v26, v2
	v_mul_f32_e32 v93, v27, v2
	v_mul_f32_e32 v94, v28, v2
	v_mul_f32_e32 v95, v29, v2
	v_bfe_u32 v96, v92, 16, 1
	v_bfe_u32 v97, v93, 16, 1
	v_bfe_u32 v98, v94, 16, 1
	v_bfe_u32 v99, v95, 16, 1
	v_add3_u32 v92, v92, v96, s72
	v_add3_u32 v93, v93, v97, s72
	v_add3_u32 v94, v94, v98, s72
	v_add3_u32 v95, v95, v99, s72
	v_perm_b32 v88, v93, v92, s6
	v_perm_b32 v89, v95, v94, s6
	v_mul_f32_e32 v92, v30, v2
	v_mul_f32_e32 v93, v31, v2
	v_mul_f32_e32 v94, v32, v2
	v_mul_f32_e32 v95, v33, v2
	v_bfe_u32 v96, v92, 16, 1
	v_bfe_u32 v97, v93, 16, 1
	v_bfe_u32 v98, v94, 16, 1
	v_bfe_u32 v99, v95, 16, 1
	v_add3_u32 v92, v92, v96, s72
	v_add3_u32 v93, v93, v97, s72
	v_add3_u32 v94, v94, v98, s72
	v_add3_u32 v95, v95, v99, s72
	v_perm_b32 v90, v93, v92, s6
	v_perm_b32 v91, v95, v94, s6
	s_nop 1
	v_permlane32_swap_b32_e32 v84, v86
	v_permlane32_swap_b32_e32 v85, v87
	v_permlane32_swap_b32_e32 v88, v90
	v_permlane32_swap_b32_e32 v89, v91
	global_store_dwordx4 v100, v[84:87], s[0:1] offset:192
	global_store_dwordx4 v100, v[88:91], s[0:1] offset:224
	s_nop 1
	v_mov_b32_e32 v4, v169
	s_max_i32 s8, s27, 8
	v_ashrrev_i32_e32 v1, 4, v4
	v_and_b32_e32 v2, 15, v4
	v_bitop3_b32 v5, v1, v2, 7 bitop3:0x6c
	v_bfe_u32 v2, v4, 2, 2
	v_lshrrev_b32_e32 v6, 1, v4
	v_lshrrev_b32_e32 v7, 1, v1
	v_and_or_b32 v2, v1, -16, v2
	v_and_b32_e32 v6, 8, v6
	v_and_b32_e32 v7, 4, v7
	v_or3_b32 v2, v2, v6, v7
	v_and_b32_e32 v6, 0x60, v4
	v_lshlrev_b32_e32 v7, 3, v4
	v_and_or_b32 v8, v7, 24, v6
	v_mov_b64_e32 v[6:7], s[94:95]
	v_readfirstlane_b32 s0, v4
	v_mad_i64_i32 v[6:7], s[2:3], v2, s74, v[6:7]
	v_lshlrev_b32_e32 v2, 1, v8
	v_lshl_add_u64 v[116:117], v[6:7], 0, v[2:3]
	s_ashr_i32 s6, s0, 6
	v_mov_b64_e32 v[6:7], s[34:35]
	v_mad_i64_i32 v[6:7], s[2:3], v1, s74, v[6:7]
	v_lshlrev_b32_e32 v2, 4, v5
	s_lshl_b32 s7, s6, 10
	s_add_i32 s1, s8, -8
	v_lshl_add_u64 v[118:119], v[6:7], 0, v[2:3]
	s_add_i32 s9, s7, 0
	s_waitcnt vmcnt(0) lgkmcnt(0)
	s_barrier
	v_mad_u64_u32 v[6:7], s[2:3], s1, v227, v[118:119]
	s_mov_b32 m0, s9
	s_sub_i32 s10, s27, s1
	global_load_lds_dwordx4 v[6:7], off
	v_lshl_add_u64 v[6:7], v[6:7], 0, s[80:81]
	s_add_i32 m0, s9, 0x2000
	v_readfirstlane_b32 s11, v187
	global_load_lds_dwordx4 v[6:7], off
	v_mad_u64_u32 v[6:7], s[2:3], s1, v227, v[116:117]
	s_add_i32 m0, s9, 0xc000
	s_nop 0
	global_load_lds_dwordx4 v[6:7], off
	v_lshl_add_u64 v[6:7], v[6:7], 0, s[80:81]
	s_add_i32 m0, s9, 0xe000
	s_cmp_lt_i32 s10, 1
	global_load_lds_dwordx4 v[6:7], off
	s_cbranch_scc1 .LBB0_866
	s_add_i32 s1, s8, -7
	v_mad_u64_u32 v[6:7], s[2:3], s1, v227, v[118:119]
	s_add_i32 m0, s9, 0x4000
	s_nop 0
	global_load_lds_dwordx4 v[6:7], off
	v_lshl_add_u64 v[6:7], v[6:7], 0, s[80:81]
	s_add_i32 m0, s9, 0x6000
	s_nop 0
	global_load_lds_dwordx4 v[6:7], off
	v_mad_u64_u32 v[6:7], s[2:3], s1, v227, v[116:117]
	s_add_i32 m0, s9, 0x10000
	s_nop 0
	global_load_lds_dwordx4 v[6:7], off
	v_lshl_add_u64 v[6:7], v[6:7], 0, s[80:81]
	s_add_i32 m0, s9, 0x12000
	s_nop 0
	global_load_lds_dwordx4 v[6:7], off

; __device__ __forceinline__ int crow(int r, int hi) { return (r & 3) + 8 * (r >> 2) + 4 * hi; }
; __device__ __forceinline__ float at_softmax(f32x16& p0, f32x16& p1, float& m_reg, f32x16& negm, float& l_reg, bf16x8& pa0, bf16x8& pa1, bf16x8& pa2, bf16x8& pa3, bool rowsel, bool use_rowsel) {
;     ...
;     float s0 = 0.f, s1 = 0.f, s2 = 0.f, s3 = 0.f;
; #pragma unroll
;     for (int r = 0; r < 16; r += 4) { p0[r] = __builtin_amdgcn_exp2f(p0[r]); p0[r + 1] = __builtin_amdgcn_exp2f(p0[r + 1]); p0[r + 2] = __builtin_amdgcn_exp2f(p0[r + 2]); p0[r + 3] = __builtin_amdgcn_exp2f(p0[r + 3]);
;         s0 += p0[r]; s1 += p0[r + 1]; s2 += p0[r + 2]; s3 += p0[r + 3]; }
; #pragma unroll
;     for (int r = 0; r < 16; r += 4) { p1[r] = __builtin_amdgcn_exp2f(p1[r]); p1[r + 1] = __builtin_amdgcn_exp2f(p1[r + 1]); p1[r + 2] = __builtin_amdgcn_exp2f(p1[r + 2]); p1[r + 3] = __builtin_amdgcn_exp2f(p1[r + 3]);
;         s0 += p1[r]; s1 += p1[r + 1]; s2 += p1[r + 2]; s3 += p1[r + 3]; }
;     float ps = (s0 + s1) + (s2 + s3);
;     if (use_rowsel && !rowsel) ps = 0.f;
;     { auto rr = __builtin_amdgcn_permlane32_swap(__float_as_uint(ps), __float_as_uint(ps), false, false); ps = __uint_as_float(rr[0]) + __uint_as_float(rr[1]); }
;     l_reg = l_reg * alpha + ps;
;     const unsigned keep = (use_rowsel && !rowsel) ? 0u : 0xffffffffu;
;     ...
;     PK4(p0, 0, pa0); PK4(p0, 8, pa1); PK4(p1, 0, pa2); PK4(p1, 8, pa3);
; template <int MODE> ...
;     ...
;         if (__any(alpha < 1.f)) { if (hi == 0) wsl[l32] = alpha; asm volatile("s_waitcnt lgkmcnt(0)" ::: "memory");
; #pragma unroll
;             for (int d = 0; d < 4; ++d)
; #pragma unroll
;                 for (int r = 0; r < 16; ++r) o[d][r] *= wsl[crow(r, hi)]; }
.LBB0_880:
	v_exp_f32_e32 v102, v102
	v_exp_f32_e32 v103, v103
	v_exp_f32_e32 v106, v106
	v_exp_f32_e32 v107, v107
	v_exp_f32_e32 v110, v110
	v_exp_f32_e32 v111, v111
	v_exp_f32_e32 v164, v100
	v_exp_f32_e32 v165, v101
	v_exp_f32_e32 v114, v114
	v_exp_f32_e32 v115, v115
	v_add_f32_e32 v166, 0, v102
	v_add_f32_e32 v167, 0, v103
	v_exp_f32_e32 v104, v104
	v_exp_f32_e32 v105, v105
	v_exp_f32_e32 v172, v86
	v_exp_f32_e32 v173, v87
	v_add_f32_e32 v166, v106, v166
	v_add_f32_e32 v167, v107, v167
	v_exp_f32_e32 v108, v108
	v_exp_f32_e32 v109, v109
	v_add_f32_e32 v166, v110, v166
	v_add_f32_e32 v167, v111, v167
	v_exp_f32_e32 v112, v112
	v_exp_f32_e32 v113, v113
	v_add_f32_e32 v100, 0, v164
	v_add_f32_e32 v101, 0, v165
	v_add_f32_e32 v166, v114, v166
	v_add_f32_e32 v167, v115, v167
	v_exp_f32_e32 v170, v84
	v_exp_f32_e32 v171, v85
	v_add_f32_e32 v100, v104, v100
	v_add_f32_e32 v101, v105, v101
	v_add_f32_e32 v86, v172, v166
	v_add_f32_e32 v87, v173, v167
	v_exp_f32_e32 v166, v88
	v_exp_f32_e32 v167, v89
	v_exp_f32_e32 v174, v90
	v_exp_f32_e32 v175, v91
	v_add_f32_e32 v100, v108, v100
	v_add_f32_e32 v101, v109, v101
	v_exp_f32_e32 v92, v92
	v_exp_f32_e32 v93, v93
	v_exp_f32_e32 v94, v94
	v_exp_f32_e32 v95, v95
	v_add_f32_e32 v100, v112, v100
	v_add_f32_e32 v101, v113, v101
	v_exp_f32_e32 v176, v96
	v_exp_f32_e32 v177, v97
	v_exp_f32_e32 v183, v98
	v_exp_f32_e32 v187, v99
	v_add_f32_e32 v84, v170, v100
	v_add_f32_e32 v85, v171, v101
	v_add_f32_e32 v84, v166, v84
	v_add_f32_e32 v85, v167, v85
	v_add_f32_e32 v86, v174, v86
	v_add_f32_e32 v87, v175, v87
	v_add_f32_e32 v84, v92, v84
	v_add_f32_e32 v85, v93, v85
	v_add_f32_e32 v86, v94, v86
	v_add_f32_e32 v87, v95, v87
	v_add_f32_e32 v84, v176, v84
	v_add_f32_e32 v85, v177, v85
	v_add_f32_e32 v86, v183, v86
	v_add_f32_e32 v87, v187, v87
	v_add_f32_e32 v84, v85, v84
	v_add_f32_e32 v85, v87, v86
	v_add_f32_e32 v100, v85, v84
	v_mov_b32_e32 v101, v100
	v_cvt_pk_bf16_f32 v84, v164, v165
	v_cvt_pk_bf16_f32 v85, v102, v103
	v_cvt_pk_bf16_f32 v86, v104, v105
	v_cvt_pk_bf16_f32 v87, v106, v107
	v_cvt_pk_bf16_f32 v88, v108, v109
	v_cvt_pk_bf16_f32 v89, v110, v111
	v_cvt_pk_bf16_f32 v90, v112, v113
	v_cvt_pk_bf16_f32 v91, v114, v115
	v_cvt_pk_bf16_f32 v96, v170, v171
	v_cvt_pk_bf16_f32 v97, v172, v173
	v_cvt_pk_bf16_f32 v98, v166, v167
	v_cvt_pk_bf16_f32 v99, v174, v175
	v_cvt_pk_bf16_f32 v92, v92, v93
	v_cvt_pk_bf16_f32 v93, v94, v95
	v_cvt_pk_bf16_f32 v94, v176, v177
	v_cvt_pk_bf16_f32 v95, v183, v187
	s_nop 1
	v_permlane32_swap_b32_e32 v100, v101
	v_permlane32_swap_b32_e32 v84, v86
	v_permlane32_swap_b32_e32 v85, v87
	v_permlane32_swap_b32_e32 v88, v90
	v_permlane32_swap_b32_e32 v89, v91
	v_permlane32_swap_b32_e32 v96, v98
	v_permlane32_swap_b32_e32 v97, v99
	v_permlane32_swap_b32_e32 v92, v94
	v_permlane32_swap_b32_e32 v93, v95
	v_cmp_gt_f32_e32 vcc, 1.0, v2
	s_cbranch_vccz .LBB0_884
	v_pk_mul_f32 v[4:5], v[4:5], v[2:3] op_sel_hi:[1,0]
	v_pk_mul_f32 v[6:7], v[6:7], v[2:3] op_sel_hi:[1,0]
	v_pk_mul_f32 v[8:9], v[8:9], v[2:3] op_sel_hi:[1,0]
	v_pk_mul_f32 v[10:11], v[10:11], v[2:3] op_sel_hi:[1,0]
	v_pk_mul_f32 v[12:13], v[12:13], v[2:3] op_sel_hi:[1,0]
	v_pk_mul_f32 v[14:15], v[14:15], v[2:3] op_sel_hi:[1,0]
	v_pk_mul_f32 v[16:17], v[16:17], v[2:3] op_sel_hi:[1,0]
	v_pk_mul_f32 v[18:19], v[18:19], v[2:3] op_sel_hi:[1,0]
	v_pk_mul_f32 v[20:21], v[20:21], v[2:3] op_sel_hi:[1,0]
	v_pk_mul_f32 v[22:23], v[22:23], v[2:3] op_sel_hi:[1,0]
	v_pk_mul_f32 v[24:25], v[24:25], v[2:3] op_sel_hi:[1,0]
	v_pk_mul_f32 v[26:27], v[26:27], v[2:3] op_sel_hi:[1,0]
	v_pk_mul_f32 v[28:29], v[28:29], v[2:3] op_sel_hi:[1,0]
	v_pk_mul_f32 v[30:31], v[30:31], v[2:3] op_sel_hi:[1,0]
	v_pk_mul_f32 v[32:33], v[32:33], v[2:3] op_sel_hi:[1,0]
	v_pk_mul_f32 v[34:35], v[34:35], v[2:3] op_sel_hi:[1,0]
	v_pk_mul_f32 v[36:37], v[36:37], v[2:3] op_sel_hi:[1,0]
	v_pk_mul_f32 v[38:39], v[38:39], v[2:3] op_sel_hi:[1,0]
	v_pk_mul_f32 v[40:41], v[40:41], v[2:3] op_sel_hi:[1,0]
	v_pk_mul_f32 v[42:43], v[42:43], v[2:3] op_sel_hi:[1,0]
	v_pk_mul_f32 v[44:45], v[44:45], v[2:3] op_sel_hi:[1,0]
	v_pk_mul_f32 v[46:47], v[46:47], v[2:3] op_sel_hi:[1,0]
	v_pk_mul_f32 v[48:49], v[48:49], v[2:3] op_sel_hi:[1,0]
	v_pk_mul_f32 v[50:51], v[50:51], v[2:3] op_sel_hi:[1,0]
	v_pk_mul_f32 v[52:53], v[52:53], v[2:3] op_sel_hi:[1,0]
	v_pk_mul_f32 v[54:55], v[54:55], v[2:3] op_sel_hi:[1,0]
	v_pk_mul_f32 v[56:57], v[56:57], v[2:3] op_sel_hi:[1,0]
	v_pk_mul_f32 v[58:59], v[58:59], v[2:3] op_sel_hi:[1,0]
	v_pk_mul_f32 v[60:61], v[60:61], v[2:3] op_sel_hi:[1,0]
	v_pk_mul_f32 v[62:63], v[62:63], v[2:3] op_sel_hi:[1,0]
	v_pk_mul_f32 v[64:65], v[64:65], v[2:3] op_sel_hi:[1,0]
	v_pk_mul_f32 v[66:67], v[66:67], v[2:3] op_sel_hi:[1,0]
; __device__ __forceinline__ int crow(int r, int hi) { return (r & 3) + 8 * (r >> 2) + 4 * hi; }
; __device__ __forceinline__ void at_pv(f32x16 (&o)[4], int vb, bf16x8 pa0, bf16x8 pa1, bf16x8 pa2, bf16x8 pa3) {
;     ...
;     PV_D0(0); PV_D0(1); PV_D0(2); PV_D0(3);
;     ...
; }
; template <int MODE> ...
;     ...
;     for (int t = 0; t < NT; ++t) {
;         const int j = jlo + t; const int buf = stg;
;         if (t + 1 < NT) asm volatile("s_waitcnt vmcnt(4)" ::: "memory"); else asm volatile("s_waitcnt vmcnt(0)" ::: "memory");
;         __builtin_amdgcn_s_barrier(); asm volatile("" ::: "memory");
;         if (t + 2 < NT) { const int s2 = stg == 0 ? 2 : stg - 1; AT_ISSUE(j + 2, s2); }
;         bool rowsel = true;
;         if (MODE == 1) rowsel = ((bmrow[j >> 5] >> (j & 31)) & 1u) != 0u;
;         if (MODE != 1 || __any(rowsel)) {
;         f32x16 p0, p1;
;         at_qkt(p0, p1, K_lds + buf * 16384, l32, hi, qr, negm);
;         const bool need_mask = MODE == 0 ? (64 * j + 63 > lim_min) : (MODE == 1 ? (64 * j + 63 > tq_min) : (64 * j + 63 > tq_min || 64 * j <= tq_min + 7 - WIN));
;         if (need_mask) at_mask<MODE>(p0, p1, 64 * j, hi, tq, lim, true);
;         bf16x8 pa0, pa1, pa2, pa3;
;         const float alpha = at_softmax(p0, p1, m_reg, negm, l_reg, pa0, pa1, pa2, pa3, rowsel, MODE == 1);
;         if (__any(alpha < 1.f)) { if (hi == 0) wsl[l32] = alpha; asm volatile("s_waitcnt lgkmcnt(0)" ::: "memory");
; #pragma unroll
;             for (int d = 0; d < 4; ++d)
; #pragma unroll
;                 for (int r = 0; r < 16; ++r) o[d][r] *= wsl[crow(r, hi)]; }
;         at_pv(o, vb0 + buf * 16384, pa0, pa1, pa2, pa3);
;         }
;         stg = stg == 2 ? 0 : stg + 1;
;     }
.LBB0_884:
	v_add_f32_e32 v100, v100, v101
	v_fmac_f32_e32 v100, v182, v2
	v_add_u32_e32 v2, s20, v129
	ds_read_b64_tr_b16 v[102:103], v2 offset:0
	ds_read_b64_tr_b16 v[104:105], v2 offset:0x800
	ds_read_b64_tr_b16 v[106:107], v2 offset:0x1000
	ds_read_b64_tr_b16 v[108:109], v2 offset:0x1800
	ds_read_b64_tr_b16 v[110:111], v2 offset:0x2000
	ds_read_b64_tr_b16 v[112:113], v2 offset:0x2800
	ds_read_b64_tr_b16 v[170:171], v2 offset:0x3000
	ds_read_b64_tr_b16 v[172:173], v2 offset:0x3800
	s_waitcnt lgkmcnt(0)
	s_add_i32 s19, s19, 1
	v_mfma_f32_32x32x16_bf16 v[4:19], v[102:105], v[84:87], v[4:19]
	ds_read_b64_tr_b16 v[102:103], v2 offset:0x200
	ds_read_b64_tr_b16 v[104:105], v2 offset:0xa00
	v_mfma_f32_32x32x16_bf16 v[4:19], v[106:109], v[88:91], v[4:19]
	ds_read_b64_tr_b16 v[106:107], v2 offset:0x1200
	ds_read_b64_tr_b16 v[108:109], v2 offset:0x1a00
	v_mfma_f32_32x32x16_bf16 v[4:19], v[110:113], v[96:99], v[4:19]
	ds_read_b64_tr_b16 v[110:111], v2 offset:0x2200
	ds_read_b64_tr_b16 v[112:113], v2 offset:0x2a00
	v_mfma_f32_32x32x16_bf16 v[4:19], v[170:173], v[92:95], v[4:19]
	ds_read_b64_tr_b16 v[170:171], v2 offset:0x3200
	ds_read_b64_tr_b16 v[172:173], v2 offset:0x3a00
	s_waitcnt lgkmcnt(0)
	v_mfma_f32_32x32x16_bf16 v[20:35], v[102:105], v[84:87], v[20:35]
	ds_read_b64_tr_b16 v[102:103], v2 offset:0x400
	ds_read_b64_tr_b16 v[104:105], v2 offset:0xc00
	v_mfma_f32_32x32x16_bf16 v[20:35], v[106:109], v[88:91], v[20:35]
	ds_read_b64_tr_b16 v[106:107], v2 offset:0x1400
	ds_read_b64_tr_b16 v[108:109], v2 offset:0x1c00
	v_mfma_f32_32x32x16_bf16 v[20:35], v[110:113], v[96:99], v[20:35]
	ds_read_b64_tr_b16 v[110:111], v2 offset:0x2400
	ds_read_b64_tr_b16 v[112:113], v2 offset:0x2c00
	v_mfma_f32_32x32x16_bf16 v[20:35], v[170:173], v[92:95], v[20:35]
	ds_read_b64_tr_b16 v[170:171], v2 offset:0x3400
	ds_read_b64_tr_b16 v[172:173], v2 offset:0x3c00
	s_waitcnt lgkmcnt(0)
	v_mfma_f32_32x32x16_bf16 v[36:51], v[102:105], v[84:87], v[36:51]
	ds_read_b64_tr_b16 v[102:103], v2 offset:0x600
	ds_read_b64_tr_b16 v[104:105], v2 offset:0xe00
	v_mfma_f32_32x32x16_bf16 v[36:51], v[106:109], v[88:91], v[36:51]
	ds_read_b64_tr_b16 v[106:107], v2 offset:0x1600
	ds_read_b64_tr_b16 v[108:109], v2 offset:0x1e00
	v_mfma_f32_32x32x16_bf16 v[36:51], v[110:113], v[96:99], v[36:51]
	ds_read_b64_tr_b16 v[110:111], v2 offset:0x2600
	ds_read_b64_tr_b16 v[112:113], v2 offset:0x2e00
	v_mfma_f32_32x32x16_bf16 v[36:51], v[170:173], v[92:95], v[36:51]
	ds_read_b64_tr_b16 v[170:171], v2 offset:0x3600
	ds_read_b64_tr_b16 v[172:173], v2 offset:0x3e00
	s_waitcnt lgkmcnt(0)
	v_mfma_f32_32x32x16_bf16 v[52:67], v[102:105], v[84:87], v[52:67]
	s_add_i32 s0, s18, 1
	s_cmp_lg_u32 s18, 2
	s_cselect_b32 s18, s0, 0
	s_add_i32 s17, s17, 64
	v_subrev_u32_e32 v180, 64, v180
	s_cmp_eq_u32 s16, s19
	v_mfma_f32_32x32x16_bf16 v[52:67], v[106:109], v[88:91], v[52:67]
	v_mfma_f32_32x32x16_bf16 v[52:67], v[110:113], v[96:99], v[52:67]
	v_mfma_f32_32x32x16_bf16 v[52:67], v[170:173], v[92:95], v[52:67]
	s_cbranch_scc1 .LBB0_887
	v_mov_b32_e32 v182, v100
	s_cmp_ge_i32 s19, s10
	s_mov_b64 s[0:1], -1
	s_cbranch_scc1 .LBB0_868
	s_branch .LBB0_869

; template <int MODE> ...
;     ...
;     asm volatile("s_waitcnt lgkmcnt(0)" ::: "memory");
;     if (hi == 0) wsl[32 + l32] = l_reg > 0.f ? 1.f / l_reg : 0.f;
.LBB0_887:
	s_waitcnt lgkmcnt(0)
	v_div_scale_f32 v2, s[2:3], v100, v100, 1.0
	v_rcp_f32_e32 v68, v2
	v_div_scale_f32 v69, vcc, 1.0, v100, 1.0
	v_fma_f32 v70, -v2, v68, 1.0
	v_fmac_f32_e32 v68, v70, v68
	v_mul_f32_e32 v70, v69, v68
	v_fma_f32 v71, -v2, v70, v69
	v_fmac_f32_e32 v70, v71, v68
	v_fma_f32 v2, -v2, v70, v69
	v_div_fmas_f32 v2, v2, v68, v70
	v_div_fixup_f32 v2, v2, v100, 1.0
	v_cmp_lt_f32_e32 vcc, 0, v100
	s_nop 1
	v_cndmask_b32_e32 v2, 0, v2, vcc
	s_branch .LBB0_790
